# plus: GQA KV loop one workgroup barrier per tile (K written in the PV segment, V after the barrier); unit-start wait keeps O stores in flight
# speedup vs baseline: 1.0094x; 1.0043x over previous
.LBB0_878:
	s_lshl_b32 s3, s2, 8
	s_add_i32 s33, s3, s29
	s_mul_i32 s8, s69, s33
	s_mul_hi_u32 s9, s68, s33
	s_add_i32 s9, s9, s8
	s_mul_i32 s8, s68, s33
	s_lshl_b64 s[8:9], s[8:9], 1
	s_add_u32 s10, s60, s8
	s_mul_i32 s8, s28, s26
	s_addc_u32 s11, s61, s9
	s_ashr_i32 s9, s8, 31
	s_lshl_b64 s[8:9], s[8:9], 1
	s_add_u32 s8, s10, s8
	s_addc_u32 s9, s11, s9
	s_abs_i32 s11, s28
	s_mul_hi_u32 s12, s11, s25
	s_mul_i32 s13, s12, s89
	s_sub_i32 s11, s11, s13
	s_ashr_i32 s10, s28, 31
	s_add_i32 s13, s12, 1
	s_sub_i32 s14, s11, s89
	s_cmp_ge_u32 s11, s89
	s_cselect_b32 s12, s13, s12
	s_cselect_b32 s11, s14, s11
	s_add_i32 s13, s12, 1
	s_cmp_ge_u32 s11, s89
	s_cselect_b32 s11, s13, s12
	s_xor_b32 s11, s11, s10
	s_waitcnt vmcnt(8)
	s_barrier
	v_mbcnt_lo_u32_b32 v0, -1, 0
	v_mbcnt_hi_u32_b32 v0, -1, v0
	s_sub_i32 s10, s11, s10
	v_add_u32_e32 v184, s80, v0
	s_mul_i32 s10, s10, s27
	s_ashr_i32 s11, s10, 31
	v_ashrrev_i32_e32 v18, 1, v184
	v_bfi_b32 v0, s84, v18, v184
	v_ashrrev_i32_e32 v1, 31, v18
	s_lshl_b64 s[12:13], s[10:11], 1
	v_mul_lo_u32 v3, s69, v0
	v_mul_lo_u32 v4, s68, v1
	v_mad_u64_u32 v[0:1], s[10:11], s68, v0, 0
	v_bfe_u32 v2, v184, 5, 1
	v_add3_u32 v1, v1, v4, v3
	v_lshl_add_u64 v[0:1], v[0:1], 1, s[8:9]
	v_lshlrev_b32_e32 v162, 4, v2
	v_mov_b32_e32 v163, v129
	v_lshl_add_u64 v[16:17], v[0:1], 0, v[162:163]
	s_add_u32 s8, s21, s12
	v_ashrrev_i32_e32 v185, 4, v184
	v_lshlrev_b32_e32 v0, 3, v184
	s_addc_u32 s9, s22, s13
	v_and_b32_e32 v186, 0x78, v0
	v_mul_lo_u32 v0, v185, s62
	s_add_u32 s10, s23, s12
	v_or_b32_e32 v1, v0, v186
	v_add_u32_e32 v0, s38, v0
	s_addc_u32 s11, s24, s13
	v_lshlrev_b32_e32 v128, 1, v1
	v_or_b32_e32 v0, v0, v186
	global_load_dwordx4 v[174:177], v[16:17], off offset:64
	global_load_dwordx4 v[156:159], v[16:17], off offset:96
	global_load_dwordx4 v[188:191], v[16:17], off offset:192
	global_load_dwordx4 v[164:167], v[16:17], off offset:224
	v_lshlrev_b32_e32 v198, 1, v0
	global_load_dwordx4 v[8:11], v128, s[10:11]
	global_load_dwordx4 v[4:7], v128, s[8:9]
	global_load_dwordx4 v[12:15], v198, s[10:11]
	global_load_dwordx4 v[0:3], v198, s[8:9]
	global_load_dwordx4 v[200:203], v[16:17], off
	global_load_dwordx4 v[204:207], v[16:17], off offset:32
	global_load_dwordx4 v[208:211], v[16:17], off offset:128
	global_load_dwordx4 v[212:215], v[16:17], off offset:160
	s_add_i32 s16, s3, 0xffffff00
	s_cmp_eq_u32 s2, 0
	s_cselect_b64 s[14:15], -1, 0
	s_and_b64 s[2:3], s[14:15], exec
	s_cselect_b32 s2, -1, s16
	v_and_b32_e32 v163, 31, v184
	v_and_b32_e32 v18, 0xffffffe0, v18
	s_max_i32 s3, s2, 0
	v_add3_u32 v16, v163, s3, v18
	v_ashrrev_i32_e32 v17, 31, v16
	v_lshlrev_b64 v[16:17], 8, v[16:17]
	v_lshl_add_u64 v[16:17], s[70:71], 0, v[16:17]
	v_and_b32_e32 v84, 32, v184
	v_mov_b32_e32 v85, v129
	v_lshl_add_u64 v[20:21], v[16:17], 0, v[84:85]
	s_mov_b32 s3, 0x80000
	v_add_co_u32_e32 v22, vcc, s3, v20
	s_mov_b64 s[16:17], 0x80040
	v_lshl_add_u64 v[16:17], v[20:21], 0, s[40:41]
	v_addc_co_u32_e32 v23, vcc, 0, v21, vcc
	v_lshl_add_u64 v[28:29], v[20:21], 0, s[16:17]
	s_mov_b64 s[16:17], 0x800c0
	global_load_dwordx4 v[60:63], v[20:21], off offset:16
	global_load_dwordx4 v[72:75], v[20:21], off
	global_load_dwordx4 v[76:79], v[22:23], off
	global_load_dwordx4 v[68:71], v[16:17], off offset:16
	global_load_dwordx4 v[48:51], v[20:21], off offset:80
	global_load_dwordx4 v[56:59], v[20:21], off offset:64
	global_load_dwordx4 v[32:35], v[20:21], off offset:144
	global_load_dwordx4 v[40:43], v[20:21], off offset:128
	v_lshl_add_u64 v[36:37], v[20:21], 0, s[44:45]
	global_load_dwordx4 v[64:67], v[22:23], off offset:64
	global_load_dwordx4 v[44:47], v[22:23], off offset:128
	global_load_dwordx4 v[16:19], v[20:21], off offset:208
	global_load_dwordx4 v[24:27], v[20:21], off offset:192
	v_lshl_add_u64 v[20:21], v[20:21], 0, s[16:17]
	global_load_dwordx4 v[52:55], v[28:29], off offset:16
	s_nop 0
	global_load_dwordx4 v[28:31], v[22:23], off offset:192
	s_nop 0
	global_load_dwordx4 v[36:39], v[36:37], off offset:16
	s_nop 0
	global_load_dwordx4 v[20:23], v[20:21], off offset:16
	global_load_dwordx4 v[142:145], v84, s[58:59]
	global_load_dwordx4 v[138:141], v84, s[58:59] offset:16
	global_load_dwordx4 v[134:137], v84, s[58:59] offset:64
	global_load_dwordx4 v[130:133], v84, s[58:59] offset:80
	global_load_dwordx4 v[124:127], v84, s[58:59] offset:128
	global_load_dwordx4 v[120:123], v84, s[58:59] offset:144
	global_load_dwordx4 v[116:119], v84, s[58:59] offset:192
	global_load_dwordx4 v[112:115], v84, s[58:59] offset:208
	global_load_dwordx4 v[104:107], v84, s[58:59] offset:272
	global_load_dwordx4 v[108:111], v84, s[58:59] offset:256
	global_load_dwordx4 v[96:99], v84, s[58:59] offset:336
	global_load_dwordx4 v[100:103], v84, s[58:59] offset:320
	global_load_dwordx4 v[88:91], v84, s[58:59] offset:400
	global_load_dwordx4 v[92:95], v84, s[58:59] offset:384
	global_load_dwordx4 v[80:83], v84, s[58:59] offset:464
	s_nop 0
	global_load_dwordx4 v[84:87], v84, s[58:59] offset:448
	s_mov_b32 s3, 0x800000
	s_cmp_lt_i32 s2, 0
	s_waitcnt vmcnt(43)
	v_and_b32_e32 v179, 0xffff0000, v177
	v_lshlrev_b32_e32 v178, 16, v177
	v_and_b32_e32 v183, 0xffff0000, v176
	s_waitcnt vmcnt(35)
	v_and_b32_e32 v177, 0xffff0000, v200
	v_lshlrev_b32_e32 v182, 16, v176
	v_lshlrev_b32_e32 v176, 16, v200
	v_mul_f32_e32 v200, v177, v177
	v_and_b32_e32 v171, 0xffff0000, v201
	v_lshlrev_b32_e32 v170, 16, v201
	v_pk_fma_f32 v[200:201], v[176:177], v[176:177], v[200:201] op_sel_hi:[1,1,0]
	v_mul_f32_e32 v224, v171, v171
	v_pk_fma_f32 v[200:201], v[170:171], v[170:171], v[200:201]
	v_and_b32_e32 v151, 0xffff0000, v165
	v_lshlrev_b32_e32 v150, 16, v165
	v_and_b32_e32 v153, 0xffff0000, v164
	v_lshlrev_b32_e32 v152, 16, v164
	v_and_b32_e32 v165, 0xffff0000, v202
	v_lshlrev_b32_e32 v164, 16, v202
	v_pk_add_f32 v[200:201], v[224:225], v[200:201] op_sel_hi:[0,1]
	v_pk_fma_f32 v[200:201], v[164:165], v[164:165], v[200:201]
	v_mul_f32_e32 v224, v165, v165
	v_and_b32_e32 v221, 0xffff0000, v203
	v_lshlrev_b32_e32 v220, 16, v203
	v_pk_add_f32 v[200:201], v[224:225], v[200:201] op_sel_hi:[0,1]
	v_pk_fma_f32 v[200:201], v[220:221], v[220:221], v[200:201]
	v_mul_f32_e32 v224, v221, v221
	s_waitcnt vmcnt(34)
	v_and_b32_e32 v217, 0xffff0000, v205
	v_lshlrev_b32_e32 v216, 16, v205
	v_and_b32_e32 v205, 0xffff0000, v204
	v_lshlrev_b32_e32 v204, 16, v204
	v_pk_add_f32 v[200:201], v[224:225], v[200:201] op_sel_hi:[0,1]
	v_pk_fma_f32 v[200:201], v[204:205], v[204:205], v[200:201]
	v_mul_f32_e32 v224, v205, v205
	v_pk_add_f32 v[200:201], v[224:225], v[200:201] op_sel_hi:[0,1]
	v_pk_fma_f32 v[200:201], v[216:217], v[216:217], v[200:201]
	v_mul_f32_e32 v224, v217, v217
	v_and_b32_e32 v147, 0xffff0000, v167
	v_lshlrev_b32_e32 v146, 16, v167
	v_and_b32_e32 v149, 0xffff0000, v166
	v_lshlrev_b32_e32 v148, 16, v166
	v_and_b32_e32 v167, 0xffff0000, v157
	v_lshlrev_b32_e32 v166, 16, v157
	v_and_b32_e32 v173, 0xffff0000, v156
	v_lshlrev_b32_e32 v172, 16, v156
	v_and_b32_e32 v157, 0xffff0000, v191
	v_lshlrev_b32_e32 v156, 16, v191
	v_and_b32_e32 v161, 0xffff0000, v190
	v_lshlrev_b32_e32 v160, 16, v190
	v_and_b32_e32 v191, 0xffff0000, v175
	v_lshlrev_b32_e32 v190, 16, v175
	v_and_b32_e32 v169, 0xffff0000, v189
	v_lshlrev_b32_e32 v168, 16, v189
	v_and_b32_e32 v193, 0xffff0000, v174
	v_lshlrev_b32_e32 v192, 16, v174
	v_and_b32_e32 v175, 0xffff0000, v188
	v_lshlrev_b32_e32 v174, 16, v188
	v_and_b32_e32 v189, 0xffff0000, v207
	v_lshlrev_b32_e32 v188, 16, v207
	v_and_b32_e32 v207, 0xffff0000, v206
	v_lshlrev_b32_e32 v206, 16, v206
	v_pk_add_f32 v[200:201], v[224:225], v[200:201] op_sel_hi:[0,1]
	v_pk_fma_f32 v[200:201], v[206:207], v[206:207], v[200:201]
	v_mul_f32_e32 v224, v207, v207
	v_pk_add_f32 v[200:201], v[224:225], v[200:201] op_sel_hi:[0,1]
	v_pk_fma_f32 v[200:201], v[188:189], v[188:189], v[200:201]
	v_mul_f32_e32 v224, v189, v189
	v_pk_add_f32 v[200:201], v[224:225], v[200:201] op_sel_hi:[0,1]
	v_pk_fma_f32 v[200:201], v[192:193], v[192:193], v[200:201]
	v_mul_f32_e32 v224, v193, v193
	v_pk_add_f32 v[200:201], v[224:225], v[200:201] op_sel_hi:[0,1]
	v_pk_fma_f32 v[200:201], v[190:191], v[190:191], v[200:201]
	v_mul_f32_e32 v224, v191, v191
	v_pk_add_f32 v[200:201], v[224:225], v[200:201] op_sel_hi:[0,1]
	v_pk_fma_f32 v[200:201], v[182:183], v[182:183], v[200:201]
	v_mul_f32_e32 v224, v183, v183
	v_pk_add_f32 v[200:201], v[224:225], v[200:201] op_sel_hi:[0,1]
	v_pk_fma_f32 v[200:201], v[178:179], v[178:179], v[200:201]
	v_mul_f32_e32 v224, v179, v179
	v_pk_add_f32 v[200:201], v[224:225], v[200:201] op_sel_hi:[0,1]
	v_pk_fma_f32 v[200:201], v[172:173], v[172:173], v[200:201]
	v_mul_f32_e32 v224, v173, v173
	v_pk_add_f32 v[200:201], v[224:225], v[200:201] op_sel_hi:[0,1]
	v_pk_fma_f32 v[200:201], v[166:167], v[166:167], v[200:201]
	v_mul_f32_e32 v224, v167, v167
	v_and_b32_e32 v155, 0xffff0000, v159
	v_lshlrev_b32_e32 v154, 16, v159
	v_and_b32_e32 v159, 0xffff0000, v158
	v_lshlrev_b32_e32 v158, 16, v158
	v_pk_add_f32 v[200:201], v[224:225], v[200:201] op_sel_hi:[0,1]
	v_pk_fma_f32 v[200:201], v[158:159], v[158:159], v[200:201]
	v_mul_f32_e32 v224, v159, v159
	v_pk_add_f32 v[200:201], v[224:225], v[200:201] op_sel_hi:[0,1]
	v_pk_fma_f32 v[200:201], v[154:155], v[154:155], v[200:201]
	v_mul_f32_e32 v224, v155, v155
	s_waitcnt vmcnt(33)
	v_and_b32_e32 v223, 0xffff0000, v211
	v_lshlrev_b32_e32 v222, 16, v211
	v_and_b32_e32 v203, 0xffff0000, v210
	v_lshlrev_b32_e32 v202, 16, v210
	v_and_b32_e32 v211, 0xffff0000, v209
	v_lshlrev_b32_e32 v210, 16, v209
	v_and_b32_e32 v209, 0xffff0000, v208
	v_lshlrev_b32_e32 v208, 16, v208
	v_pk_add_f32 v[200:201], v[224:225], v[200:201] op_sel_hi:[0,1]
	v_pk_fma_f32 v[200:201], v[208:209], v[208:209], v[200:201]
	v_mul_f32_e32 v224, v209, v209
	v_pk_add_f32 v[200:201], v[224:225], v[200:201] op_sel_hi:[0,1]
	v_pk_fma_f32 v[200:201], v[210:211], v[210:211], v[200:201]
	v_mul_f32_e32 v224, v211, v211
	v_pk_add_f32 v[200:201], v[224:225], v[200:201] op_sel_hi:[0,1]
	v_pk_fma_f32 v[200:201], v[202:203], v[202:203], v[200:201]
	v_mul_f32_e32 v224, v203, v203
	v_pk_add_f32 v[200:201], v[224:225], v[200:201] op_sel_hi:[0,1]
	v_pk_fma_f32 v[200:201], v[222:223], v[222:223], v[200:201]
	v_mul_f32_e32 v224, v223, v223
	s_waitcnt vmcnt(32)
	v_and_b32_e32 v219, 0xffff0000, v213
	v_lshlrev_b32_e32 v218, 16, v213
	v_and_b32_e32 v213, 0xffff0000, v212
	v_lshlrev_b32_e32 v212, 16, v212
	v_pk_add_f32 v[200:201], v[224:225], v[200:201] op_sel_hi:[0,1]
	v_pk_fma_f32 v[200:201], v[212:213], v[212:213], v[200:201]
	v_mul_f32_e32 v224, v213, v213
	v_pk_add_f32 v[200:201], v[224:225], v[200:201] op_sel_hi:[0,1]
	v_pk_fma_f32 v[200:201], v[218:219], v[218:219], v[200:201]
	v_mul_f32_e32 v224, v219, v219
	v_and_b32_e32 v181, 0xffff0000, v215
	v_lshlrev_b32_e32 v180, 16, v215
	v_and_b32_e32 v215, 0xffff0000, v214
	v_lshlrev_b32_e32 v214, 16, v214
	v_pk_add_f32 v[200:201], v[224:225], v[200:201] op_sel_hi:[0,1]
	v_pk_fma_f32 v[200:201], v[214:215], v[214:215], v[200:201]
	v_mul_f32_e32 v224, v215, v215
	v_pk_add_f32 v[200:201], v[224:225], v[200:201] op_sel_hi:[0,1]
	v_pk_fma_f32 v[200:201], v[180:181], v[180:181], v[200:201]
	v_mul_f32_e32 v224, v181, v181
	v_pk_add_f32 v[200:201], v[224:225], v[200:201] op_sel_hi:[0,1]
	v_pk_fma_f32 v[200:201], v[174:175], v[174:175], v[200:201]
	v_mul_f32_e32 v224, v175, v175
	v_pk_add_f32 v[200:201], v[224:225], v[200:201] op_sel_hi:[0,1]
	v_pk_fma_f32 v[200:201], v[168:169], v[168:169], v[200:201]
	v_mul_f32_e32 v224, v169, v169
	v_pk_add_f32 v[200:201], v[224:225], v[200:201] op_sel_hi:[0,1]
	v_pk_fma_f32 v[200:201], v[160:161], v[160:161], v[200:201]
	v_mul_f32_e32 v224, v161, v161
	v_pk_add_f32 v[200:201], v[224:225], v[200:201] op_sel_hi:[0,1]
	v_pk_fma_f32 v[200:201], v[156:157], v[156:157], v[200:201]
	v_mul_f32_e32 v224, v157, v157
	v_pk_add_f32 v[200:201], v[224:225], v[200:201] op_sel_hi:[0,1]
	v_pk_fma_f32 v[200:201], v[152:153], v[152:153], v[200:201]
	v_mul_f32_e32 v224, v153, v153
	v_pk_add_f32 v[200:201], v[224:225], v[200:201] op_sel_hi:[0,1]
	v_pk_fma_f32 v[200:201], v[150:151], v[150:151], v[200:201]
	v_mul_f32_e32 v224, v151, v151
	v_pk_add_f32 v[200:201], v[224:225], v[200:201] op_sel_hi:[0,1]
	v_pk_fma_f32 v[200:201], v[148:149], v[148:149], v[200:201]
	v_mul_f32_e32 v224, v149, v149
	v_pk_add_f32 v[200:201], v[224:225], v[200:201] op_sel_hi:[0,1]
	v_pk_fma_f32 v[200:201], v[146:147], v[146:147], v[200:201]
	v_mul_f32_e32 v224, v147, v147
	v_pk_add_f32 v[200:201], v[224:225], v[200:201] op_sel_hi:[0,1]
	v_mov_b32_e32 v187, v200
	s_nop 1
	v_permlane32_swap_b32_e32 v200, v187
	v_add_f32_e32 v187, v200, v187
	v_fmamk_f32 v187, v187, 0x3c000000, v248
	v_mul_f32_e32 v194, 0x4b800000, v187
	v_cmp_gt_f32_e32 vcc, s3, v187
	s_nop 1
	v_cndmask_b32_e32 v187, v187, v194, vcc
	v_rsq_f32_e32 v187, v187
	s_nop 0
	v_mul_f32_e32 v194, 0x45800000, v187
	v_cndmask_b32_e32 v200, v187, v194, vcc
	v_mul_f32_e32 v200, 0x3e0293ee, v200
	s_waitcnt vmcnt(15)
	v_pk_mul_f32 v[142:143], v[142:143], v[200:201] op_sel_hi:[1,0]
	s_waitcnt vmcnt(13)
	v_pk_mul_f32 v[134:135], v[134:135], v[200:201] op_sel_hi:[1,0]
	v_pk_mul_f32 v[176:177], v[142:143], v[176:177]
	v_pk_mul_f32 v[142:143], v[144:145], v[200:201] op_sel_hi:[1,0]
	s_waitcnt vmcnt(12)
	v_pk_mul_f32 v[130:131], v[130:131], v[200:201] op_sel_hi:[1,0]
	v_pk_mul_f32 v[170:171], v[142:143], v[170:171]
	v_pk_mul_f32 v[142:143], v[134:135], v[204:205]
	v_pk_mul_f32 v[134:135], v[136:137], v[200:201] op_sel_hi:[1,0]
	s_waitcnt vmcnt(11)
	v_pk_mul_f32 v[124:125], v[124:125], v[200:201] op_sel_hi:[1,0]
	v_pk_mul_f32 v[136:137], v[134:135], v[216:217]
	v_pk_mul_f32 v[134:135], v[130:131], v[206:207]
	v_pk_mul_f32 v[130:131], v[132:133], v[200:201] op_sel_hi:[1,0]
	s_waitcnt vmcnt(10)
	v_pk_mul_f32 v[120:121], v[120:121], v[200:201] op_sel_hi:[1,0]
	v_pk_mul_f32 v[132:133], v[130:131], v[188:189]
	v_pk_mul_f32 v[130:131], v[124:125], v[192:193]
	v_pk_mul_f32 v[124:125], v[126:127], v[200:201] op_sel_hi:[1,0]
	s_waitcnt vmcnt(9)
	v_pk_mul_f32 v[116:117], v[116:117], v[200:201] op_sel_hi:[1,0]
	v_pk_mul_f32 v[126:127], v[124:125], v[190:191]
	v_pk_mul_f32 v[124:125], v[120:121], v[182:183]
	v_pk_mul_f32 v[120:121], v[122:123], v[200:201] op_sel_hi:[1,0]
	v_pk_mul_f32 v[138:139], v[138:139], v[200:201] op_sel_hi:[1,0]
	v_pk_mul_f32 v[122:123], v[120:121], v[178:179]
	v_pk_mul_f32 v[120:121], v[116:117], v[172:173]
	v_pk_mul_f32 v[116:117], v[118:119], v[200:201] op_sel_hi:[1,0]
	s_waitcnt vmcnt(8)
	v_pk_mul_f32 v[112:113], v[112:113], v[200:201] op_sel_hi:[1,0]
	v_pk_mul_f32 v[164:165], v[138:139], v[164:165]
	v_pk_mul_f32 v[138:139], v[140:141], v[200:201] op_sel_hi:[1,0]
	v_pk_mul_f32 v[118:119], v[116:117], v[166:167]
	v_pk_mul_f32 v[116:117], v[112:113], v[158:159]
	v_pk_mul_f32 v[112:113], v[114:115], v[200:201] op_sel_hi:[1,0]
	s_waitcnt vmcnt(6)
	v_pk_mul_f32 v[108:109], v[200:201], v[108:109] op_sel_hi:[0,1]
	v_pk_mul_f32 v[110:111], v[200:201], v[110:111] op_sel_hi:[0,1]
	v_pk_mul_f32 v[104:105], v[200:201], v[104:105] op_sel_hi:[0,1]
	v_pk_mul_f32 v[106:107], v[200:201], v[106:107] op_sel_hi:[0,1]
	s_waitcnt vmcnt(4)
	v_pk_mul_f32 v[100:101], v[200:201], v[100:101] op_sel_hi:[0,1]
	v_pk_mul_f32 v[102:103], v[200:201], v[102:103] op_sel_hi:[0,1]
	v_pk_mul_f32 v[96:97], v[200:201], v[96:97] op_sel_hi:[0,1]
	v_pk_mul_f32 v[98:99], v[200:201], v[98:99] op_sel_hi:[0,1]
	s_waitcnt vmcnt(2)
	v_pk_mul_f32 v[92:93], v[200:201], v[92:93] op_sel_hi:[0,1]
	v_pk_mul_f32 v[94:95], v[200:201], v[94:95] op_sel_hi:[0,1]
	v_pk_mul_f32 v[88:89], v[200:201], v[88:89] op_sel_hi:[0,1]
	v_pk_mul_f32 v[90:91], v[200:201], v[90:91] op_sel_hi:[0,1]
	s_waitcnt vmcnt(0)
	v_pk_mul_f32 v[84:85], v[200:201], v[84:85] op_sel_hi:[0,1]
	v_pk_mul_f32 v[86:87], v[200:201], v[86:87] op_sel_hi:[0,1]
	v_pk_mul_f32 v[80:81], v[200:201], v[80:81] op_sel_hi:[0,1]
	v_pk_mul_f32 v[82:83], v[200:201], v[82:83] op_sel_hi:[0,1]
	v_pk_mul_f32 v[144:145], v[138:139], v[220:221]
	v_pk_mul_f32 v[112:113], v[112:113], v[154:155]
	v_pk_mul_f32 v[108:109], v[108:109], v[208:209]
	v_pk_mul_f32 v[110:111], v[110:111], v[210:211]
	v_pk_mul_f32 v[104:105], v[104:105], v[202:203]
	v_pk_mul_f32 v[106:107], v[106:107], v[222:223]
	v_pk_mul_f32 v[100:101], v[100:101], v[212:213]
	v_pk_mul_f32 v[102:103], v[102:103], v[218:219]
	v_pk_mul_f32 v[96:97], v[96:97], v[214:215]
	v_pk_mul_f32 v[98:99], v[98:99], v[180:181]
	v_pk_mul_f32 v[92:93], v[92:93], v[174:175]
	v_pk_mul_f32 v[94:95], v[94:95], v[168:169]
	v_pk_mul_f32 v[88:89], v[88:89], v[160:161]
	v_pk_mul_f32 v[90:91], v[90:91], v[156:157]
	v_pk_mul_f32 v[84:85], v[84:85], v[152:153]
	v_pk_mul_f32 v[86:87], v[86:87], v[150:151]
	v_pk_mul_f32 v[80:81], v[80:81], v[148:149]
	v_pk_mul_f32 v[82:83], v[82:83], v[146:147]
	s_cbranch_scc1 .LBB0_880
	v_pk_mul_f32 v[114:115], v[76:77], v[108:109]
	v_pk_mul_f32 v[76:77], v[76:77], v[176:177]
	v_pk_fma_f32 v[114:115], v[72:73], v[176:177], v[114:115] neg_lo:[0,0,1] neg_hi:[0,0,1]
	v_pk_fma_f32 v[108:109], v[72:73], v[108:109], v[76:77]
	v_pk_mul_f32 v[72:73], v[78:79], v[110:111]
	v_pk_mul_f32 v[76:77], v[78:79], v[170:171]
	v_pk_fma_f32 v[72:73], v[74:75], v[170:171], v[72:73] neg_lo:[0,0,1] neg_hi:[0,0,1]
	v_pk_fma_f32 v[110:111], v[74:75], v[110:111], v[76:77]
	v_pk_mul_f32 v[74:75], v[68:69], v[104:105]
	v_mov_b64_e32 v[170:171], v[72:73]
	v_pk_fma_f32 v[74:75], v[60:61], v[164:165], v[74:75] neg_lo:[0,0,1] neg_hi:[0,0,1]
	v_pk_mul_f32 v[60:61], v[60:61], v[104:105]
	v_mov_b64_e32 v[176:177], v[114:115]
	v_pk_fma_f32 v[104:105], v[68:69], v[164:165], v[60:61]
	v_pk_mul_f32 v[60:61], v[70:71], v[106:107]
	v_mov_b64_e32 v[164:165], v[74:75]
	v_pk_fma_f32 v[60:61], v[62:63], v[144:145], v[60:61] neg_lo:[0,0,1] neg_hi:[0,0,1]
	v_pk_mul_f32 v[62:63], v[62:63], v[106:107]
	s_nop 0
	v_pk_fma_f32 v[106:107], v[70:71], v[144:145], v[62:63]
	v_pk_mul_f32 v[62:63], v[64:65], v[100:101]
	v_mov_b64_e32 v[144:145], v[60:61]
	v_pk_fma_f32 v[62:63], v[56:57], v[142:143], v[62:63] neg_lo:[0,0,1] neg_hi:[0,0,1]
	v_pk_mul_f32 v[56:57], v[56:57], v[100:101]
	s_nop 0
	v_pk_fma_f32 v[100:101], v[64:65], v[142:143], v[56:57]
	v_pk_mul_f32 v[56:57], v[66:67], v[102:103]
	v_mov_b64_e32 v[142:143], v[62:63]
	v_pk_fma_f32 v[56:57], v[58:59], v[136:137], v[56:57] neg_lo:[0,0,1] neg_hi:[0,0,1]
	v_pk_mul_f32 v[58:59], v[58:59], v[102:103]
	s_nop 0
	v_pk_fma_f32 v[102:103], v[66:67], v[136:137], v[58:59]
	v_pk_mul_f32 v[58:59], v[52:53], v[96:97]
	v_mov_b64_e32 v[136:137], v[56:57]
	v_pk_fma_f32 v[58:59], v[48:49], v[134:135], v[58:59] neg_lo:[0,0,1] neg_hi:[0,0,1]
	v_pk_mul_f32 v[48:49], v[48:49], v[96:97]
	s_nop 0
	v_pk_fma_f32 v[96:97], v[52:53], v[134:135], v[48:49]
	v_pk_mul_f32 v[48:49], v[54:55], v[98:99]
	v_mov_b64_e32 v[134:135], v[58:59]
	v_pk_fma_f32 v[48:49], v[50:51], v[132:133], v[48:49] neg_lo:[0,0,1] neg_hi:[0,0,1]
	v_pk_mul_f32 v[50:51], v[50:51], v[98:99]
	s_nop 0
	v_pk_fma_f32 v[98:99], v[54:55], v[132:133], v[50:51]
	v_pk_mul_f32 v[50:51], v[44:45], v[92:93]
	v_mov_b64_e32 v[132:133], v[48:49]
	v_pk_fma_f32 v[50:51], v[40:41], v[130:131], v[50:51] neg_lo:[0,0,1] neg_hi:[0,0,1]
	v_pk_mul_f32 v[40:41], v[40:41], v[92:93]
	s_nop 0
	v_pk_fma_f32 v[92:93], v[44:45], v[130:131], v[40:41]
	v_pk_mul_f32 v[40:41], v[46:47], v[94:95]
	v_mov_b64_e32 v[130:131], v[50:51]
	v_pk_fma_f32 v[40:41], v[42:43], v[126:127], v[40:41] neg_lo:[0,0,1] neg_hi:[0,0,1]
	v_pk_mul_f32 v[42:43], v[42:43], v[94:95]
	s_nop 0
	v_pk_fma_f32 v[94:95], v[46:47], v[126:127], v[42:43]
	v_pk_mul_f32 v[42:43], v[36:37], v[88:89]
	v_mov_b64_e32 v[126:127], v[40:41]
	v_pk_fma_f32 v[42:43], v[32:33], v[124:125], v[42:43] neg_lo:[0,0,1] neg_hi:[0,0,1]
	v_pk_mul_f32 v[32:33], v[32:33], v[88:89]
	s_nop 0
	v_pk_fma_f32 v[88:89], v[36:37], v[124:125], v[32:33]
	v_pk_mul_f32 v[32:33], v[38:39], v[90:91]
	v_mov_b64_e32 v[124:125], v[42:43]
	v_pk_fma_f32 v[32:33], v[34:35], v[122:123], v[32:33] neg_lo:[0,0,1] neg_hi:[0,0,1]
	v_pk_mul_f32 v[34:35], v[34:35], v[90:91]
	s_nop 0
	v_pk_fma_f32 v[90:91], v[38:39], v[122:123], v[34:35]
	v_pk_mul_f32 v[34:35], v[28:29], v[84:85]
	v_mov_b64_e32 v[122:123], v[32:33]
	v_pk_fma_f32 v[34:35], v[24:25], v[120:121], v[34:35] neg_lo:[0,0,1] neg_hi:[0,0,1]
	v_pk_mul_f32 v[24:25], v[24:25], v[84:85]
	s_nop 0
	v_pk_fma_f32 v[84:85], v[28:29], v[120:121], v[24:25]
	v_pk_mul_f32 v[24:25], v[30:31], v[86:87]
	v_mov_b64_e32 v[120:121], v[34:35]
	v_pk_fma_f32 v[24:25], v[26:27], v[118:119], v[24:25] neg_lo:[0,0,1] neg_hi:[0,0,1]
	v_pk_mul_f32 v[26:27], v[26:27], v[86:87]
	s_nop 0
	v_pk_fma_f32 v[86:87], v[30:31], v[118:119], v[26:27]
	v_pk_mul_f32 v[26:27], v[20:21], v[80:81]
	v_mov_b64_e32 v[118:119], v[24:25]
	v_pk_fma_f32 v[26:27], v[16:17], v[116:117], v[26:27] neg_lo:[0,0,1] neg_hi:[0,0,1]
	v_pk_mul_f32 v[16:17], v[16:17], v[80:81]
	s_nop 0
	v_pk_fma_f32 v[80:81], v[20:21], v[116:117], v[16:17]
	v_pk_mul_f32 v[16:17], v[22:23], v[82:83]
	v_mov_b64_e32 v[116:117], v[26:27]
	v_pk_fma_f32 v[16:17], v[18:19], v[112:113], v[16:17] neg_lo:[0,0,1] neg_hi:[0,0,1]
	v_pk_mul_f32 v[18:19], v[18:19], v[82:83]
	s_nop 0
	v_pk_fma_f32 v[82:83], v[22:23], v[112:113], v[18:19]
	v_mov_b64_e32 v[112:113], v[16:17]
.LBB0_880:
	v_add_u32_e32 v21, 32, v185
	v_and_b32_e32 v17, 0xfffff0, v185
	v_lshlrev_b32_e32 v18, 1, v185
	v_and_b32_e32 v22, 0xfffff0, v21
	v_lshlrev_b32_e32 v23, 1, v21
	v_and_b32_e32 v16, 63, v184
	v_and_or_b32 v17, v18, 8, v17
	v_and_or_b32 v22, v23, 8, v22
	v_lshrrev_b32_e32 v17, 1, v17
	v_lshrrev_b32_e32 v19, 5, v186
	v_lshrrev_b32_e32 v22, 1, v22
	v_lshlrev_b32_e32 v23, 4, v16
	v_lshrrev_b32_e32 v18, 1, v185
	v_or_b32_e32 v17, v17, v19
	v_and_b32_e32 v20, 3, v185
	v_or_b32_e32 v19, v22, v19
	v_lshlrev_b32_e32 v22, 3, v16
	v_and_b32_e32 v23, 0xc0, v23
	v_lshlrev_b32_e32 v16, 1, v16
	v_and_or_b32 v18, v18, 4, v20
	v_lshlrev_b32_e32 v20, 1, v186
	v_and_or_b32 v23, v22, 24, v23
	v_and_b32_e32 v16, 32, v16
	v_and_b32_e32 v22, 0x100, v22
	v_lshlrev_b32_e32 v17, 9, v17
	v_lshlrev_b32_e32 v18, 6, v18
	v_or3_b32 v114, v23, v16, v22
	v_and_b32_e32 v16, 48, v20
	v_or3_b32 v17, v17, v18, v16
	v_add_u32_e32 v212, 0, v17
	v_lshlrev_b32_e32 v19, 9, v19
	v_cvt_pk_bf16_f32 v138, v176, v177
	v_cvt_pk_bf16_f32 v139, v170, v171
	v_cvt_pk_bf16_f32 v140, v164, v165
	v_cvt_pk_bf16_f32 v141, v144, v145
	v_cvt_pk_bf16_f32 v154, v142, v143
	v_cvt_pk_bf16_f32 v155, v136, v137
	v_cvt_pk_bf16_f32 v156, v134, v135
	v_cvt_pk_bf16_f32 v157, v132, v133
	v_cvt_pk_bf16_f32 v158, v130, v131
	v_cvt_pk_bf16_f32 v159, v126, v127
	v_cvt_pk_bf16_f32 v160, v124, v125
	v_cvt_pk_bf16_f32 v161, v122, v123
	v_cvt_pk_bf16_f32 v150, v120, v121
	v_cvt_pk_bf16_f32 v151, v118, v119
	v_cvt_pk_bf16_f32 v152, v116, v117
	v_cvt_pk_bf16_f32 v153, v112, v113
	v_cvt_pk_bf16_f32 v146, v108, v109
	v_cvt_pk_bf16_f32 v147, v110, v111
	v_cvt_pk_bf16_f32 v148, v104, v105
	v_cvt_pk_bf16_f32 v149, v106, v107
	v_cvt_pk_bf16_f32 v142, v100, v101
	v_cvt_pk_bf16_f32 v143, v102, v103
	v_cvt_pk_bf16_f32 v144, v96, v97
	v_cvt_pk_bf16_f32 v145, v98, v99
	v_cvt_pk_bf16_f32 v134, v92, v93
	v_cvt_pk_bf16_f32 v135, v94, v95
	v_cvt_pk_bf16_f32 v136, v88, v89
	v_cvt_pk_bf16_f32 v137, v90, v91
	v_cvt_pk_bf16_f32 v130, v84, v85
	v_cvt_pk_bf16_f32 v131, v86, v87
	v_cvt_pk_bf16_f32 v132, v80, v81
	v_cvt_pk_bf16_f32 v133, v82, v83
	s_waitcnt vmcnt(0)
	ds_write_b128 v212, v[8:11]
	v_lshlrev_b32_e32 v8, 8, v185
	v_and_b32_e32 v9, 0x70, v184
	v_or3_b32 v16, v19, v18, v16
	v_bitop3_b32 v8, v20, v8, v9 bitop3:0xde
	v_add_u32_e32 v213, 0, v16
	v_add_u32_e32 v214, 0, v8
	ds_write_b128 v213, v[12:15]
	ds_write_b128 v214, v[4:7] offset:32768
	v_lshlrev_b32_e32 v4, 8, v21
	v_bitop3_b32 v4, v20, v4, v9 bitop3:0xde
	v_add_u32_e32 v215, 0, v4
	ds_write_b128 v215, v[0:3] offset:32768
	v_lshlrev_b32_e32 v0, 4, v163
	v_lshlrev_b32_e32 v56, 8, v163
	v_and_b32_e32 v57, 0x70, v0
	v_bitop3_b32 v0, v162, v56, v57 bitop3:0xde
	v_add_u32_e32 v216, 0, v0
	s_waitcnt lgkmcnt(0)
	s_barrier
	ds_read_b128 v[16:19], v216 offset:32768
	ds_read_b128 v[20:23], v216 offset:40960
	s_waitcnt lgkmcnt(1)
	v_mfma_f32_32x32x16_bf16 v[32:47], v[16:19], v[138:141], 0
	v_or_b32_e32 v48, 32, v162
	v_bitop3_b32 v48, v48, v56, v57 bitop3:0xde
	v_add_u32_e32 v218, 0, v48
	ds_read_b128 v[48:51], v218 offset:32768
	ds_read_b128 v[52:55], v218 offset:40960
	s_cmp_lg_u32 0, -1
	s_cselect_b32 s53, 0, 0
	s_add_u32 s16, s10, s96
	s_waitcnt lgkmcnt(2)
	v_mfma_f32_32x32x16_bf16 v[16:31], v[20:23], v[138:141], 0
	s_addc_u32 s17, s11, s97
	v_mov_b32_e32 v199, v129
	s_add_u32 s18, s8, s96
	s_addc_u32 s19, s9, s97
	v_lshl_add_u64 v[60:61], s[18:19], 0, v[198:199]
	s_add_u32 s2, s16, s96
	s_addc_u32 s3, s17, s97
	s_waitcnt lgkmcnt(1)
	v_mfma_f32_32x32x16_bf16 v[32:47], v[48:51], v[154:157], v[32:47]
	v_or_b32_e32 v48, 64, v162
	v_bitop3_b32 v48, v48, v56, v57 bitop3:0xde
	v_add_u32_e32 v219, 0, v48
	v_lshl_add_u64 v[64:65], s[2:3], 0, v[128:129]
	s_mov_b32 s72, s73
	s_mov_b32 s74, s73
	s_mov_b32 s75, s73
	s_waitcnt lgkmcnt(0)
	v_mfma_f32_32x32x16_bf16 v[16:31], v[52:55], v[154:157], v[16:31]
	ds_read_b128 v[48:51], v219 offset:32768
	ds_read_b128 v[52:55], v219 offset:40960
	s_mov_b32 s76, s73
	s_mov_b32 s77, s73
	s_mov_b32 s78, s73
	s_mov_b32 s79, s73
	s_mov_b32 s80, s73
	s_mov_b32 s81, s73
	s_waitcnt lgkmcnt(1)
	v_mfma_f32_32x32x16_bf16 v[32:47], v[48:51], v[158:161], v[32:47]
	v_or_b32_e32 v48, 0x60, v162
	v_bitop3_b32 v48, v48, v56, v57 bitop3:0xde
	v_add_u32_e32 v220, 0, v48
	s_mov_b32 s82, s73
	s_mov_b32 s83, s73
	s_mov_b32 s84, s73
	s_mov_b32 s85, s73
	s_waitcnt lgkmcnt(0)
	v_mfma_f32_32x32x16_bf16 v[16:31], v[52:55], v[158:161], v[16:31]
	ds_read_b128 v[48:51], v220 offset:32768
	ds_read_b128 v[52:55], v220 offset:40960
	s_mov_b32 s86, s73
	s_mov_b32 s87, s73
	v_mov_b64_e32 v[0:1], s[72:73]
	v_mov_b64_e32 v[14:15], s[86:87]
	v_add_u32_e32 v209, s53, v114
	v_mov_b64_e32 v[2:3], s[74:75]
	s_waitcnt lgkmcnt(1)
	v_mfma_f32_32x32x16_bf16 v[32:47], v[48:51], v[150:153], v[32:47]
	v_or_b32_e32 v48, 0x80, v162
	v_bitop3_b32 v48, v48, v56, v57 bitop3:0xde
	v_add_u32_e32 v221, 0, v48
	v_mov_b64_e32 v[4:5], s[76:77]
	v_mov_b64_e32 v[6:7], s[78:79]
	v_mov_b64_e32 v[8:9], s[80:81]
	v_mov_b64_e32 v[10:11], s[82:83]
	s_waitcnt lgkmcnt(0)
	v_mfma_f32_32x32x16_bf16 v[16:31], v[52:55], v[150:153], v[16:31]
	ds_read_b128 v[48:51], v221 offset:32768
	ds_read_b128 v[52:55], v221 offset:40960
	v_mov_b64_e32 v[12:13], s[84:85]
	s_mov_b32 s39, 4
	v_mov_b32_e32 v217, 0
	v_readlane_b32 s80, v255, 48
	s_movk_i32 s79, 0xff
	s_movk_i32 s84, 0xffe0
	s_waitcnt lgkmcnt(1)
	v_mfma_f32_32x32x16_bf16 v[32:47], v[48:51], v[146:149], v[32:47]
	v_or_b32_e32 v48, 0xa0, v162
	v_bitop3_b32 v48, v48, v56, v57 bitop3:0xde
	v_add_u32_e32 v222, 0, v48
	s_waitcnt lgkmcnt(0)
	v_mfma_f32_32x32x16_bf16 v[16:31], v[52:55], v[146:149], v[16:31]
	ds_read_b128 v[48:51], v222 offset:32768
	ds_read_b128 v[52:55], v222 offset:40960
	s_waitcnt lgkmcnt(1)
	v_mfma_f32_32x32x16_bf16 v[32:47], v[48:51], v[142:145], v[32:47]
	v_or_b32_e32 v48, 0xc0, v162
	v_bitop3_b32 v48, v48, v56, v57 bitop3:0xde
	v_add_u32_e32 v224, 0, v48
	s_waitcnt lgkmcnt(0)
	v_mfma_f32_32x32x16_bf16 v[16:31], v[52:55], v[142:145], v[16:31]
	ds_read_b128 v[48:51], v224 offset:32768
	ds_read_b128 v[52:55], v224 offset:40960
	s_waitcnt lgkmcnt(1)
	v_mfma_f32_32x32x16_bf16 v[32:47], v[48:51], v[134:137], v[32:47]
	v_or_b32_e32 v48, 0xe0, v162
	v_bitop3_b32 v48, v48, v56, v57 bitop3:0xde
	v_add_u32_e32 v223, 0, v48
	v_lshl_add_u64 v[56:57], s[18:19], 0, v[128:129]
	s_waitcnt lgkmcnt(0)
	v_mfma_f32_32x32x16_bf16 v[16:31], v[52:55], v[134:137], v[16:31]
	ds_read_b128 v[48:51], v223 offset:32768
	ds_read_b128 v[52:55], v223 offset:40960
	global_load_dwordx4 v[56:59], v[56:57], off
	s_nop 0
	global_load_dwordx4 v[60:63], v[60:61], off
	s_nop 0
	global_load_dwordx4 v[162:165], v[64:65], off
	v_lshl_add_u64 v[64:65], s[2:3], 0, v[198:199]
	s_waitcnt lgkmcnt(1)
	v_mfma_f32_32x32x16_bf16 v[32:47], v[48:51], v[130:133], v[32:47]
	global_load_dwordx4 v[166:169], v[64:65], off
	s_waitcnt lgkmcnt(0)
	v_mfma_f32_32x32x16_bf16 v[16:31], v[52:55], v[130:133], v[16:31]
	s_nop 8
	v_lshl_add_u64 v[48:49], s[16:17], 0, v[128:129]
	global_load_dwordx4 v[48:51], v[48:49], off
	v_lshl_add_u64 v[52:53], s[16:17], 0, v[198:199]
	global_load_dwordx4 v[52:55], v[52:53], off
	s_add_u32 s16, s18, s96
	s_addc_u32 s17, s19, s97
	v_lshl_add_u64 v[64:65], s[16:17], 0, v[128:129]
	global_load_dwordx4 v[170:173], v[64:65], off
	v_lshl_add_u64 v[64:65], s[16:17], 0, v[198:199]
	global_load_dwordx4 v[174:177], v[64:65], off
	s_and_b64 s[2:3], s[14:15], exec
	s_cselect_b32 s14, 3, 35
	s_waitcnt vmcnt(4)
	s_waitcnt vmcnt(3)
	ds_write_b128 v212, v[48:51] offset:16384
	s_waitcnt vmcnt(2)
	ds_write_b128 v213, v[52:55] offset:16384
	v_mov_b32_e32 v178, v48
	v_mov_b32_e32 v179, v49
	v_mov_b32_e32 v180, v50
	v_mov_b32_e32 v181, v51
	v_mov_b32_e32 v182, v52
	v_mov_b32_e32 v183, v53
	v_mov_b32_e32 v184, v54
	v_mov_b32_e32 v185, v55
	ds_write_b128 v214, v[56:59] offset:49152
	ds_write_b128 v215, v[60:63] offset:49152
	v_exp_f32_e32 v64, v32
	v_exp_f32_e32 v65, v33
	v_exp_f32_e32 v66, v34
	v_exp_f32_e32 v67, v35
	v_exp_f32_e32 v68, v36
	v_exp_f32_e32 v69, v37
	v_exp_f32_e32 v70, v38
	v_exp_f32_e32 v71, v39
	v_exp_f32_e32 v72, v40
	v_exp_f32_e32 v73, v41
	v_exp_f32_e32 v74, v42
	v_exp_f32_e32 v80, v16
	v_exp_f32_e32 v81, v17
	v_exp_f32_e32 v75, v43
	v_exp_f32_e32 v76, v44
	v_exp_f32_e32 v77, v45
	v_exp_f32_e32 v78, v46
	v_exp_f32_e32 v79, v47
	v_exp_f32_e32 v82, v18
	v_exp_f32_e32 v83, v19
	v_lshl_add_u64 v[16:17], s[12:13], 0, v[128:129]
	v_lshl_add_u64 v[18:19], s[12:13], 0, v[198:199]
	v_exp_f32_e32 v94, v30
	v_exp_f32_e32 v95, v31
	v_exp_f32_e32 v92, v28
	v_exp_f32_e32 v93, v29
	v_exp_f32_e32 v196, v26
	v_exp_f32_e32 v197, v27
	v_exp_f32_e32 v194, v24
	v_exp_f32_e32 v195, v25
	v_exp_f32_e32 v86, v22
	v_exp_f32_e32 v87, v23
	v_exp_f32_e32 v84, v20
	v_exp_f32_e32 v85, v21
	s_addk_i32 s53, 0x4000
	v_lshl_add_u64 v[200:201], s[64:65], 0, v[16:17]
	v_lshl_add_u64 v[202:203], s[64:65], 0, v[18:19]
	v_lshl_add_u64 v[204:205], s[66:67], 0, v[16:17]
	v_lshl_add_u64 v[206:207], s[66:67], 0, v[18:19]
	v_mov_b64_e32 v[62:63], v[14:15]
	v_mov_b64_e32 v[46:47], v[14:15]
	v_mov_b64_e32 v[30:31], v[14:15]
	v_add_u32_e32 v211, s53, v114
	v_mov_b64_e32 v[60:61], v[12:13]
	v_mov_b64_e32 v[58:59], v[10:11]
	v_mov_b64_e32 v[56:57], v[8:9]
	v_mov_b64_e32 v[54:55], v[6:7]
	v_mov_b64_e32 v[52:53], v[4:5]
	v_mov_b64_e32 v[50:51], v[2:3]
	v_mov_b64_e32 v[48:49], v[0:1]
	v_mov_b64_e32 v[44:45], v[12:13]
	v_mov_b64_e32 v[42:43], v[10:11]
	v_mov_b64_e32 v[40:41], v[8:9]
	v_mov_b64_e32 v[38:39], v[6:7]
	v_mov_b64_e32 v[36:37], v[4:5]
	v_mov_b64_e32 v[34:35], v[2:3]
	v_mov_b64_e32 v[32:33], v[0:1]
	v_mov_b64_e32 v[28:29], v[12:13]
	v_mov_b64_e32 v[26:27], v[10:11]
	v_mov_b64_e32 v[24:25], v[8:9]
	v_mov_b64_e32 v[22:23], v[6:7]
	v_mov_b64_e32 v[20:21], v[4:5]
	v_mov_b64_e32 v[18:19], v[2:3]
	v_mov_b64_e32 v[16:17], v[0:1]
	s_mov_b32 s53, 0x38e38e39
	s_waitcnt lgkmcnt(0)
	s_barrier
.LBB0_881:
	ds_read_b128 v[96:99], v216 offset:49152
	ds_read_b128 v[100:103], v216 offset:57344
	ds_write_b128 v212, v[178:181] offset:16384
	ds_write_b128 v213, v[182:185] offset:16384
	ds_read_b128 v[178:181], v218 offset:49152
	ds_read_b128 v[182:185], v218 offset:57344
	s_waitcnt lgkmcnt(5)
	v_mfma_f32_32x32x16_bf16 v[112:127], v[96:99], v[138:141], 0
	s_waitcnt lgkmcnt(4)
	v_mfma_f32_32x32x16_bf16 v[96:111], v[100:103], v[138:141], 0
	s_waitcnt lgkmcnt(1)
	v_mfma_f32_32x32x16_bf16 v[112:127], v[178:181], v[154:157], v[112:127]
	s_waitcnt lgkmcnt(0)
	v_mfma_f32_32x32x16_bf16 v[96:111], v[182:185], v[154:157], v[96:111]
	ds_read_b128 v[178:181], v219 offset:49152
	ds_read_b128 v[182:185], v219 offset:57344
	s_waitcnt lgkmcnt(1)
	v_mfma_f32_32x32x16_bf16 v[112:127], v[178:181], v[158:161], v[112:127]
	s_waitcnt lgkmcnt(0)
	v_mfma_f32_32x32x16_bf16 v[96:111], v[182:185], v[158:161], v[96:111]
	ds_read_b128 v[178:181], v220 offset:49152
	ds_read_b128 v[182:185], v220 offset:57344
	s_waitcnt lgkmcnt(1)
	v_mfma_f32_32x32x16_bf16 v[112:127], v[178:181], v[150:153], v[112:127]
	s_waitcnt lgkmcnt(0)
	v_mfma_f32_32x32x16_bf16 v[96:111], v[182:185], v[150:153], v[96:111]
	ds_read_b128 v[178:181], v221 offset:49152
	ds_read_b128 v[182:185], v221 offset:57344
	s_waitcnt lgkmcnt(1)
	v_mfma_f32_32x32x16_bf16 v[112:127], v[178:181], v[146:149], v[112:127]
	s_waitcnt lgkmcnt(0)
	v_mfma_f32_32x32x16_bf16 v[96:111], v[182:185], v[146:149], v[96:111]
	ds_read_b128 v[178:181], v222 offset:49152
	ds_read_b128 v[182:185], v222 offset:57344
	s_waitcnt lgkmcnt(1)
	v_mfma_f32_32x32x16_bf16 v[112:127], v[178:181], v[142:145], v[112:127]
	s_waitcnt lgkmcnt(0)
	v_mfma_f32_32x32x16_bf16 v[96:111], v[182:185], v[142:145], v[96:111]
	ds_read_b128 v[178:181], v224 offset:49152
	ds_read_b128 v[182:185], v224 offset:57344
	s_waitcnt lgkmcnt(1)
	v_mfma_f32_32x32x16_bf16 v[112:127], v[178:181], v[134:137], v[112:127]
	s_waitcnt lgkmcnt(0)
	v_mfma_f32_32x32x16_bf16 v[96:111], v[182:185], v[134:137], v[96:111]
	ds_read_b128 v[178:181], v223 offset:49152
	ds_read_b128 v[182:185], v223 offset:57344
	s_waitcnt lgkmcnt(1)
	v_mfma_f32_32x32x16_bf16 v[112:127], v[178:181], v[130:133], v[112:127]
	v_add_f32_e32 v88, v64, v65
	v_add_f32_e32 v89, v72, v73
	v_add_f32_e32 v90, v80, v81
	v_add_f32_e32 v91, v194, v195
	v_add_f32_e32 v88, v66, v88
	v_add_f32_e32 v89, v74, v89
	v_add_f32_e32 v90, v82, v90
	v_add_f32_e32 v91, v196, v91
	v_add_f32_e32 v88, v67, v88
	v_add_f32_e32 v89, v75, v89
	v_add_f32_e32 v90, v83, v90
	v_add_f32_e32 v91, v197, v91
	v_add_f32_e32 v88, v68, v88
	v_add_f32_e32 v89, v76, v89
	v_add_f32_e32 v90, v84, v90
	v_add_f32_e32 v91, v92, v91
	v_add_f32_e32 v88, v69, v88
	v_add_f32_e32 v89, v77, v89
	v_add_f32_e32 v90, v85, v90
	v_add_f32_e32 v91, v93, v91
	v_add_f32_e32 v88, v70, v88
	v_add_f32_e32 v89, v78, v89
	v_add_f32_e32 v90, v86, v90
	v_add_f32_e32 v91, v94, v91
	v_add_f32_e32 v88, v71, v88
	v_add_f32_e32 v89, v79, v89
	v_add_f32_e32 v90, v87, v90
	v_add_f32_e32 v91, v95, v91
	v_add_f32_e32 v88, v89, v88
	v_add_f32_e32 v89, v91, v90
	v_add_f32_e32 v227, v88, v89
	v_mov_b32_e32 v228, v227
	v_cvt_pk_bf16_f32 v88, v64, v65
	v_cvt_pk_bf16_f32 v89, v66, v67
	v_cvt_pk_bf16_f32 v90, v68, v69
	v_cvt_pk_bf16_f32 v91, v70, v71
	s_nop 1
	v_permlane32_swap_b32_e32 v227, v228
	v_permlane32_swap_b32_e32 v88, v90
	v_permlane32_swap_b32_e32 v89, v91
	v_cvt_pk_bf16_f32 v72, v72, v73
	v_cvt_pk_bf16_f32 v73, v74, v75
	v_cvt_pk_bf16_f32 v74, v76, v77
	v_cvt_pk_bf16_f32 v75, v78, v79
	v_cvt_pk_bf16_f32 v64, v80, v81
	v_cvt_pk_bf16_f32 v65, v82, v83
	v_cvt_pk_bf16_f32 v66, v84, v85
	v_cvt_pk_bf16_f32 v67, v86, v87
	v_cvt_pk_bf16_f32 v68, v194, v195
	v_cvt_pk_bf16_f32 v69, v196, v197
	v_cvt_pk_bf16_f32 v70, v92, v93
	v_cvt_pk_bf16_f32 v71, v94, v95
	s_waitcnt lgkmcnt(0)
	v_mfma_f32_32x32x16_bf16 v[96:111], v[182:185], v[130:133], v[96:111]
	v_permlane32_swap_b32_e32 v72, v74
	v_permlane32_swap_b32_e32 v73, v75
	v_permlane32_swap_b32_e32 v64, v66
	v_permlane32_swap_b32_e32 v65, v67
	v_permlane32_swap_b32_e32 v68, v70
	v_permlane32_swap_b32_e32 v69, v71
	s_add_i32 s2, s39, -1
	s_mul_i32 s2, s2, s62
	s_lshl_b32 s72, s2, 6
	s_lshl_b64 s[2:3], s[72:73], 1
	s_add_u32 s12, s10, s2
	s_addc_u32 s13, s11, s3
	s_add_u32 s2, s8, s2
	s_addc_u32 s3, s9, s3
	global_load_dwordx4 v[178:181], v128, s[12:13]
	global_load_dwordx4 v[182:185], v198, s[12:13]
	global_load_dwordx4 v[186:189], v128, s[2:3]
	global_load_dwordx4 v[190:193], v198, s[2:3]
	ds_read_b64_tr_b16 v[76:77], v209 offset:0
	ds_read_b64_tr_b16 v[78:79], v209 offset:0x800
	ds_read_b64_tr_b16 v[80:81], v209 offset:0x1000
	ds_read_b64_tr_b16 v[82:83], v209 offset:0x1800
	ds_read_b64_tr_b16 v[84:85], v209 offset:0x2000
	ds_read_b64_tr_b16 v[86:87], v209 offset:0x2800
	ds_read_b64_tr_b16 v[92:93], v209 offset:0x3000
	ds_read_b64_tr_b16 v[94:95], v209 offset:0x3800
	s_waitcnt lgkmcnt(0)
	s_nop 0
	v_mfma_f32_32x32x16_bf16 v[0:15], v[76:79], v[88:91], v[0:15]
	v_mfma_f32_32x32x16_bf16 v[0:15], v[80:83], v[72:75], v[0:15]
	v_mfma_f32_32x32x16_bf16 v[0:15], v[84:87], v[64:67], v[0:15]
	ds_read_b64_tr_b16 v[76:77], v209 offset:0x200
	ds_read_b64_tr_b16 v[78:79], v209 offset:0xa00
	ds_read_b64_tr_b16 v[80:81], v209 offset:0x1200
	v_mfma_f32_32x32x16_bf16 v[0:15], v[92:95], v[68:71], v[0:15]
	ds_read_b64_tr_b16 v[82:83], v209 offset:0x1a00
	ds_read_b64_tr_b16 v[84:85], v209 offset:0x2200
	ds_read_b64_tr_b16 v[86:87], v209 offset:0x2a00
	ds_read_b64_tr_b16 v[92:93], v209 offset:0x3200
	ds_read_b64_tr_b16 v[94:95], v209 offset:0x3a00
	s_waitcnt lgkmcnt(0)
	v_mfma_f32_32x32x16_bf16 v[48:63], v[76:79], v[88:91], v[48:63]
	v_mfma_f32_32x32x16_bf16 v[48:63], v[80:83], v[72:75], v[48:63]
	v_mfma_f32_32x32x16_bf16 v[48:63], v[84:87], v[64:67], v[48:63]
	ds_read_b64_tr_b16 v[76:77], v209 offset:0x400
	ds_read_b64_tr_b16 v[78:79], v209 offset:0xc00
	ds_read_b64_tr_b16 v[80:81], v209 offset:0x1400
	ds_read_b64_tr_b16 v[82:83], v209 offset:0x1c00
	v_mfma_f32_32x32x16_bf16 v[48:63], v[92:95], v[68:71], v[48:63]
	ds_read_b64_tr_b16 v[84:85], v209 offset:0x2400
	ds_read_b64_tr_b16 v[86:87], v209 offset:0x2c00
	ds_read_b64_tr_b16 v[92:93], v209 offset:0x3400
	ds_read_b64_tr_b16 v[94:95], v209 offset:0x3c00
	s_waitcnt lgkmcnt(0)
	v_mfma_f32_32x32x16_bf16 v[32:47], v[76:79], v[88:91], v[32:47]
	ds_read_b64_tr_b16 v[76:77], v209 offset:0x600
	ds_read_b64_tr_b16 v[78:79], v209 offset:0xe00
	s_waitcnt vmcnt(4)
	ds_write_b128 v214, v[170:173] offset:32768
	ds_write_b128 v215, v[174:177] offset:32768
	v_exp_f32_e32 v234, v104
	v_exp_f32_e32 v235, v105
	v_exp_f32_e32 v236, v106
	v_exp_f32_e32 v237, v107
	v_exp_f32_e32 v238, v108
	v_exp_f32_e32 v239, v109
	v_exp_f32_e32 v240, v110
	v_exp_f32_e32 v241, v111
	v_mfma_f32_32x32x16_bf16 v[32:47], v[80:83], v[72:75], v[32:47]
	v_exp_f32_e32 v80, v112
	v_exp_f32_e32 v81, v113
	v_exp_f32_e32 v82, v114
	v_exp_f32_e32 v83, v115
	v_mfma_f32_32x32x16_bf16 v[32:47], v[84:87], v[64:67], v[32:47]
	v_exp_f32_e32 v84, v116
	v_exp_f32_e32 v85, v117
	v_exp_f32_e32 v86, v118
	v_exp_f32_e32 v87, v119
	v_exp_f32_e32 v112, v96
	v_exp_f32_e32 v113, v97
	v_exp_f32_e32 v114, v98
	v_exp_f32_e32 v115, v99
	v_exp_f32_e32 v116, v100
	v_exp_f32_e32 v117, v101
	v_exp_f32_e32 v118, v102
	v_exp_f32_e32 v119, v103
	v_mfma_f32_32x32x16_bf16 v[32:47], v[92:95], v[68:71], v[32:47]
	ds_read_b64_tr_b16 v[92:93], v209 offset:0x1600
	ds_read_b64_tr_b16 v[94:95], v209 offset:0x1e00
	ds_read_b64_tr_b16 v[96:97], v209 offset:0x2600
	ds_read_b64_tr_b16 v[98:99], v209 offset:0x2e00
	ds_read_b64_tr_b16 v[100:101], v209 offset:0x3600
	ds_read_b64_tr_b16 v[102:103], v209 offset:0x3e00
	s_waitcnt lgkmcnt(0)
	v_mfma_f32_32x32x16_bf16 v[16:31], v[76:79], v[88:91], v[16:31]
	v_exp_f32_e32 v88, v120
	v_exp_f32_e32 v89, v121
	v_exp_f32_e32 v90, v122
	v_exp_f32_e32 v91, v123
	v_mfma_f32_32x32x16_bf16 v[16:31], v[92:95], v[72:75], v[16:31]
	v_exp_f32_e32 v92, v124
	v_exp_f32_e32 v93, v125
	v_exp_f32_e32 v94, v126
	v_exp_f32_e32 v95, v127
	s_barrier
	v_mfma_f32_32x32x16_bf16 v[16:31], v[96:99], v[64:67], v[16:31]
	v_mfma_f32_32x32x16_bf16 v[16:31], v[100:103], v[68:71], v[16:31]
.LBB0_883:
	s_waitcnt lgkmcnt(0)
	ds_read_b128 v[64:67], v216 offset:32768
	ds_read_b128 v[68:71], v216 offset:40960
	ds_write_b128 v212, v[162:165]
	ds_write_b128 v213, v[166:169]
	ds_read_b128 v[162:165], v218 offset:32768
	ds_read_b128 v[166:169], v218 offset:40960
	s_waitcnt lgkmcnt(5)
	v_mfma_f32_32x32x16_bf16 v[96:111], v[64:67], v[138:141], 0
	s_waitcnt lgkmcnt(4)
	v_mfma_f32_32x32x16_bf16 v[64:79], v[68:71], v[138:141], 0
	s_waitcnt lgkmcnt(1)
	v_mfma_f32_32x32x16_bf16 v[96:111], v[162:165], v[154:157], v[96:111]
	s_waitcnt lgkmcnt(0)
	v_mfma_f32_32x32x16_bf16 v[64:79], v[166:169], v[154:157], v[64:79]
	ds_read_b128 v[162:165], v219 offset:32768
	ds_read_b128 v[166:169], v219 offset:40960
	s_waitcnt lgkmcnt(1)
	v_mfma_f32_32x32x16_bf16 v[96:111], v[162:165], v[158:161], v[96:111]
	s_waitcnt lgkmcnt(0)
	v_mfma_f32_32x32x16_bf16 v[64:79], v[166:169], v[158:161], v[64:79]
	ds_read_b128 v[162:165], v220 offset:32768
	ds_read_b128 v[166:169], v220 offset:40960
	s_waitcnt lgkmcnt(1)
	v_mfma_f32_32x32x16_bf16 v[96:111], v[162:165], v[150:153], v[96:111]
	s_waitcnt lgkmcnt(0)
	v_mfma_f32_32x32x16_bf16 v[64:79], v[166:169], v[150:153], v[64:79]
	ds_read_b128 v[162:165], v221 offset:32768
	ds_read_b128 v[166:169], v221 offset:40960
	s_waitcnt lgkmcnt(1)
	v_mfma_f32_32x32x16_bf16 v[96:111], v[162:165], v[146:149], v[96:111]
	s_waitcnt lgkmcnt(0)
	v_mfma_f32_32x32x16_bf16 v[64:79], v[166:169], v[146:149], v[64:79]
	ds_read_b128 v[162:165], v222 offset:32768
	ds_read_b128 v[166:169], v222 offset:40960
	s_waitcnt lgkmcnt(1)
	v_mfma_f32_32x32x16_bf16 v[96:111], v[162:165], v[142:145], v[96:111]
	s_waitcnt lgkmcnt(0)
	v_mfma_f32_32x32x16_bf16 v[64:79], v[166:169], v[142:145], v[64:79]
	ds_read_b128 v[162:165], v224 offset:32768
	ds_read_b128 v[166:169], v224 offset:40960
	s_waitcnt lgkmcnt(1)
	v_mfma_f32_32x32x16_bf16 v[96:111], v[162:165], v[134:137], v[96:111]
	s_waitcnt lgkmcnt(0)
	v_mfma_f32_32x32x16_bf16 v[64:79], v[166:169], v[134:137], v[64:79]
	ds_read_b128 v[162:165], v223 offset:32768
	ds_read_b128 v[166:169], v223 offset:40960
	s_waitcnt lgkmcnt(1)
	v_mfma_f32_32x32x16_bf16 v[96:111], v[162:165], v[130:133], v[96:111]
	v_add_f32_e32 v120, v80, v81
	v_add_f32_e32 v121, v88, v89
	v_add_f32_e32 v122, v112, v113
	s_waitcnt lgkmcnt(0)
	v_mfma_f32_32x32x16_bf16 v[64:79], v[166:169], v[130:133], v[64:79]
	v_add_f32_e32 v123, v234, v235
	v_add_f32_e32 v120, v82, v120
	v_add_f32_e32 v121, v90, v121
	v_add_f32_e32 v122, v114, v122
	v_add_f32_e32 v123, v236, v123
	v_add_f32_e32 v120, v83, v120
	v_add_f32_e32 v121, v91, v121
	v_add_f32_e32 v122, v115, v122
	v_add_f32_e32 v123, v237, v123
	v_add_f32_e32 v120, v84, v120
	v_add_f32_e32 v121, v92, v121
	v_add_f32_e32 v122, v116, v122
	v_add_f32_e32 v123, v238, v123
	v_add_f32_e32 v120, v85, v120
	v_add_f32_e32 v121, v93, v121
	v_add_f32_e32 v122, v117, v122
	v_add_f32_e32 v123, v239, v123
	v_add_f32_e32 v120, v86, v120
	v_add_f32_e32 v121, v94, v121
	v_add_f32_e32 v122, v118, v122
	v_add_f32_e32 v123, v240, v123
	v_add_f32_e32 v120, v87, v120
	v_add_f32_e32 v121, v95, v121
	v_add_f32_e32 v122, v119, v122
	v_add_f32_e32 v123, v241, v123
	v_add_f32_e32 v120, v121, v120
	v_add_f32_e32 v121, v123, v122
	v_add_f32_e32 v229, v120, v121
	v_mov_b32_e32 v233, v229
	s_nop 1
	v_permlane32_swap_b32_e32 v229, v233
	v_cvt_pk_bf16_f32 v124, v80, v81
	v_cvt_pk_bf16_f32 v125, v82, v83
	v_cvt_pk_bf16_f32 v126, v84, v85
	v_cvt_pk_bf16_f32 v127, v86, v87
	v_cvt_pk_bf16_f32 v120, v88, v89
	v_cvt_pk_bf16_f32 v121, v90, v91
	v_cvt_pk_bf16_f32 v122, v92, v93
	v_cvt_pk_bf16_f32 v123, v94, v95
	v_cvt_pk_bf16_f32 v112, v112, v113
	v_cvt_pk_bf16_f32 v113, v114, v115
	v_cvt_pk_bf16_f32 v114, v116, v117
	v_cvt_pk_bf16_f32 v115, v118, v119
	v_cvt_pk_bf16_f32 v116, v234, v235
	v_cvt_pk_bf16_f32 v117, v236, v237
	v_cvt_pk_bf16_f32 v118, v238, v239
	v_cvt_pk_bf16_f32 v119, v240, v241
	s_nop 0
	v_permlane32_swap_b32_e32 v124, v126
	v_permlane32_swap_b32_e32 v125, v127
	v_permlane32_swap_b32_e32 v120, v122
	v_permlane32_swap_b32_e32 v121, v123
	v_permlane32_swap_b32_e32 v112, v114
	v_permlane32_swap_b32_e32 v113, v115
	v_permlane32_swap_b32_e32 v116, v118
	v_permlane32_swap_b32_e32 v117, v119
	s_min_i32 s2, s39, s14
	s_mul_i32 s2, s2, s62
	s_lshl_b32 s72, s2, 6
	s_lshl_b64 s[2:3], s[72:73], 1
	s_add_u32 s12, s10, s2
	s_addc_u32 s13, s11, s3
	s_add_u32 s2, s8, s2
	s_addc_u32 s3, s9, s3
	global_load_dwordx4 v[162:165], v128, s[12:13]
	global_load_dwordx4 v[166:169], v198, s[12:13]
	global_load_dwordx4 v[170:173], v128, s[2:3]
	global_load_dwordx4 v[174:177], v198, s[2:3]
	ds_read_b64_tr_b16 v[80:81], v211 offset:0
	ds_read_b64_tr_b16 v[82:83], v211 offset:0x800
	ds_read_b64_tr_b16 v[84:85], v211 offset:0x1000
	ds_read_b64_tr_b16 v[86:87], v211 offset:0x1800
	ds_read_b64_tr_b16 v[88:89], v211 offset:0x2000
	ds_read_b64_tr_b16 v[90:91], v211 offset:0x2800
	ds_read_b64_tr_b16 v[92:93], v211 offset:0x3000
	ds_read_b64_tr_b16 v[94:95], v211 offset:0x3800
	s_waitcnt lgkmcnt(0)
	s_nop 0
	v_mfma_f32_32x32x16_bf16 v[0:15], v[80:83], v[124:127], v[0:15]
	v_mfma_f32_32x32x16_bf16 v[0:15], v[84:87], v[120:123], v[0:15]
	v_mfma_f32_32x32x16_bf16 v[0:15], v[88:91], v[112:115], v[0:15]
	ds_read_b64_tr_b16 v[80:81], v211 offset:0x200
	ds_read_b64_tr_b16 v[82:83], v211 offset:0xa00
	ds_read_b64_tr_b16 v[84:85], v211 offset:0x1200
	v_mfma_f32_32x32x16_bf16 v[0:15], v[92:95], v[116:119], v[0:15]
	ds_read_b64_tr_b16 v[86:87], v211 offset:0x1a00
	ds_read_b64_tr_b16 v[88:89], v211 offset:0x2200
	ds_read_b64_tr_b16 v[90:91], v211 offset:0x2a00
	ds_read_b64_tr_b16 v[92:93], v211 offset:0x3200
	ds_read_b64_tr_b16 v[94:95], v211 offset:0x3a00
	s_waitcnt lgkmcnt(0)
	v_mfma_f32_32x32x16_bf16 v[48:63], v[80:83], v[124:127], v[48:63]
	v_mfma_f32_32x32x16_bf16 v[48:63], v[84:87], v[120:123], v[48:63]
	v_mfma_f32_32x32x16_bf16 v[48:63], v[88:91], v[112:115], v[48:63]
	ds_read_b64_tr_b16 v[80:81], v211 offset:0x400
	ds_read_b64_tr_b16 v[82:83], v211 offset:0xc00
	ds_read_b64_tr_b16 v[84:85], v211 offset:0x1400
	ds_read_b64_tr_b16 v[86:87], v211 offset:0x1c00
	v_mfma_f32_32x32x16_bf16 v[48:63], v[92:95], v[116:119], v[48:63]
	ds_read_b64_tr_b16 v[88:89], v211 offset:0x2400
	ds_read_b64_tr_b16 v[90:91], v211 offset:0x2c00
	ds_read_b64_tr_b16 v[92:93], v211 offset:0x3400
	ds_read_b64_tr_b16 v[94:95], v211 offset:0x3c00
	s_waitcnt lgkmcnt(0)
	v_mfma_f32_32x32x16_bf16 v[32:47], v[80:83], v[124:127], v[32:47]
	v_exp_f32_e32 v80, v64
	v_exp_f32_e32 v81, v65
	v_exp_f32_e32 v64, v96
	v_exp_f32_e32 v65, v97
	v_exp_f32_e32 v82, v66
	v_exp_f32_e32 v83, v67
	v_exp_f32_e32 v66, v98
	v_exp_f32_e32 v67, v99
	v_mfma_f32_32x32x16_bf16 v[32:47], v[84:87], v[120:123], v[32:47]
	v_exp_f32_e32 v84, v68
	v_exp_f32_e32 v85, v69
	v_exp_f32_e32 v68, v100
	v_exp_f32_e32 v69, v101
	v_exp_f32_e32 v86, v70
	v_exp_f32_e32 v87, v71
	v_exp_f32_e32 v70, v102
	v_exp_f32_e32 v71, v103
	v_mfma_f32_32x32x16_bf16 v[32:47], v[88:91], v[112:115], v[32:47]
	v_exp_f32_e32 v194, v72
	v_exp_f32_e32 v195, v73
	ds_read_b64_tr_b16 v[72:73], v211 offset:0x600
	v_exp_f32_e32 v196, v74
	v_exp_f32_e32 v197, v75
	ds_read_b64_tr_b16 v[74:75], v211 offset:0xe00
	s_waitcnt vmcnt(4)
	ds_write_b128 v214, v[186:189] offset:49152
	ds_write_b128 v215, v[190:193] offset:49152
	v_mfma_f32_32x32x16_bf16 v[32:47], v[92:95], v[116:119], v[32:47]
	v_exp_f32_e32 v92, v76
	v_exp_f32_e32 v93, v77
	ds_read_b64_tr_b16 v[76:77], v211 offset:0x1600
	v_exp_f32_e32 v94, v78
	v_exp_f32_e32 v95, v79
	ds_read_b64_tr_b16 v[78:79], v211 offset:0x1e00
	ds_read_b64_tr_b16 v[96:97], v211 offset:0x2600
	ds_read_b64_tr_b16 v[98:99], v211 offset:0x2e00
	ds_read_b64_tr_b16 v[100:101], v211 offset:0x3600
	ds_read_b64_tr_b16 v[102:103], v211 offset:0x3e00
	s_waitcnt lgkmcnt(0)
	v_mfma_f32_32x32x16_bf16 v[16:31], v[72:75], v[124:127], v[16:31]
	v_exp_f32_e32 v72, v104
	v_exp_f32_e32 v73, v105
	v_exp_f32_e32 v74, v106
	v_exp_f32_e32 v75, v107
	v_mfma_f32_32x32x16_bf16 v[16:31], v[76:79], v[120:123], v[16:31]
	v_exp_f32_e32 v76, v108
	v_exp_f32_e32 v77, v109
	v_exp_f32_e32 v78, v110
	v_exp_f32_e32 v79, v111
	s_barrier
	v_mfma_f32_32x32x16_bf16 v[16:31], v[96:99], v[112:115], v[16:31]
	v_mfma_f32_32x32x16_bf16 v[16:31], v[100:103], v[116:119], v[16:31]
.LBB0_885:
	v_add_f32_e32 v96, v227, v228
	v_add_f32_e32 v96, v96, v217
	v_add_f32_e32 v217, v229, v233
	s_add_i32 s2, s39, 2
	s_add_i32 s3, s39, -1
	v_add_f32_e32 v217, v217, v96
	s_cmp_ge_u32 s3, s14
	s_waitcnt lgkmcnt(0)
	s_cbranch_scc1 .LBB0_887
	s_mov_b32 s39, s2
	s_branch .LBB0_881
.LBB0_887:
	ds_read_b128 v[96:99], v216 offset:49152
	ds_read_b128 v[100:103], v216 offset:57344
	ds_write_b128 v212, v[178:181] offset:16384
	ds_write_b128 v213, v[182:185] offset:16384
	s_waitcnt lgkmcnt(3)
	v_mfma_f32_32x32x16_bf16 v[112:127], v[96:99], v[138:141], 0
	s_waitcnt lgkmcnt(2)
	v_mfma_f32_32x32x16_bf16 v[96:111], v[100:103], v[138:141], 0
	ds_read_b128 v[138:141], v218 offset:49152
	s_waitcnt vmcnt(3)
	ds_read_b128 v[162:165], v218 offset:57344
	v_add_f32_e32 v128, v64, v65
	v_add_f32_e32 v128, v66, v128
	s_waitcnt lgkmcnt(1)
	v_mfma_f32_32x32x16_bf16 v[112:127], v[138:141], v[154:157], v[112:127]
	v_add_f32_e32 v128, v67, v128
	v_add_f32_e32 v128, v68, v128
	v_add_f32_e32 v128, v69, v128
	v_add_f32_e32 v128, v70, v128
	v_add_f32_e32 v128, v71, v128
	s_waitcnt lgkmcnt(0)
	v_mfma_f32_32x32x16_bf16 v[96:111], v[162:165], v[154:157], v[96:111]
	ds_read_b128 v[138:141], v219 offset:49152
	ds_read_b128 v[154:157], v219 offset:57344
	s_waitcnt lgkmcnt(1)
	v_mfma_f32_32x32x16_bf16 v[112:127], v[138:141], v[158:161], v[112:127]
	s_waitcnt lgkmcnt(0)
	v_mfma_f32_32x32x16_bf16 v[96:111], v[154:157], v[158:161], v[96:111]
	ds_read_b128 v[138:141], v220 offset:49152
	ds_read_b128 v[154:157], v220 offset:57344
	s_waitcnt lgkmcnt(1)
	v_mfma_f32_32x32x16_bf16 v[112:127], v[138:141], v[150:153], v[112:127]
	s_waitcnt lgkmcnt(0)
	v_mfma_f32_32x32x16_bf16 v[96:111], v[154:157], v[150:153], v[96:111]
	ds_read_b128 v[138:141], v221 offset:49152
	ds_read_b128 v[150:153], v221 offset:57344
	s_waitcnt lgkmcnt(1)
	v_mfma_f32_32x32x16_bf16 v[112:127], v[138:141], v[146:149], v[112:127]
	s_waitcnt lgkmcnt(0)
	v_mfma_f32_32x32x16_bf16 v[96:111], v[150:153], v[146:149], v[96:111]
	ds_read_b128 v[138:141], v222 offset:49152
	ds_read_b128 v[146:149], v222 offset:57344
	s_waitcnt lgkmcnt(1)
	v_mfma_f32_32x32x16_bf16 v[112:127], v[138:141], v[142:145], v[112:127]
	s_waitcnt lgkmcnt(0)
	v_mfma_f32_32x32x16_bf16 v[96:111], v[146:149], v[142:145], v[96:111]
	ds_read_b128 v[138:141], v224 offset:49152
	ds_read_b128 v[142:145], v224 offset:57344
	s_waitcnt lgkmcnt(1)
	v_mfma_f32_32x32x16_bf16 v[112:127], v[138:141], v[134:137], v[112:127]
	s_waitcnt lgkmcnt(0)
	v_mfma_f32_32x32x16_bf16 v[96:111], v[142:145], v[134:137], v[96:111]
	ds_read_b128 v[134:137], v223 offset:49152
	ds_read_b128 v[138:141], v223 offset:57344
	s_waitcnt lgkmcnt(1)
	v_mfma_f32_32x32x16_bf16 v[112:127], v[134:137], v[130:133], v[112:127]
	s_waitcnt lgkmcnt(0)
	v_mfma_f32_32x32x16_bf16 v[96:111], v[138:141], v[130:133], v[96:111]
	v_add_f32_e32 v130, v72, v73
	v_add_f32_e32 v131, v80, v81
	v_add_f32_e32 v132, v194, v195
	v_add_f32_e32 v130, v74, v130
	v_add_f32_e32 v131, v82, v131
	v_add_f32_e32 v132, v196, v132
	v_add_f32_e32 v130, v75, v130
	v_add_f32_e32 v131, v83, v131
	v_add_f32_e32 v132, v197, v132
	v_add_f32_e32 v130, v76, v130
	v_add_f32_e32 v131, v84, v131
	v_add_f32_e32 v132, v92, v132
	v_add_f32_e32 v130, v77, v130
	v_add_f32_e32 v131, v85, v131
	v_add_f32_e32 v132, v93, v132
	v_add_f32_e32 v130, v78, v130
	v_add_f32_e32 v131, v86, v131
	v_add_f32_e32 v132, v94, v132
	v_add_f32_e32 v130, v79, v130
	v_add_f32_e32 v131, v87, v131
	v_add_f32_e32 v132, v95, v132
	v_add_f32_e32 v128, v130, v128
	v_add_f32_e32 v130, v132, v131
	v_add_f32_e32 v142, v128, v130
	v_mov_b32_e32 v143, v142
	v_cvt_pk_bf16_f32 v130, v64, v65
	v_cvt_pk_bf16_f32 v131, v66, v67
	v_cvt_pk_bf16_f32 v132, v68, v69
	v_cvt_pk_bf16_f32 v133, v70, v71
	v_cvt_pk_bf16_f32 v72, v72, v73
	v_cvt_pk_bf16_f32 v73, v74, v75
	v_cvt_pk_bf16_f32 v74, v76, v77
	v_cvt_pk_bf16_f32 v75, v78, v79
	s_nop 1
	v_permlane32_swap_b32_e32 v142, v143
	v_permlane32_swap_b32_e32 v72, v74
	v_permlane32_swap_b32_e32 v73, v75
	v_cvt_pk_bf16_f32 v138, v80, v81
	v_cvt_pk_bf16_f32 v139, v82, v83
	v_cvt_pk_bf16_f32 v140, v84, v85
	v_cvt_pk_bf16_f32 v141, v86, v87
	v_cvt_pk_bf16_f32 v134, v194, v195
	v_cvt_pk_bf16_f32 v135, v196, v197
	v_cvt_pk_bf16_f32 v136, v92, v93
	v_cvt_pk_bf16_f32 v137, v94, v95
	v_permlane32_swap_b32_e32 v130, v132
	v_permlane32_swap_b32_e32 v131, v133
	v_permlane32_swap_b32_e32 v138, v140
	v_permlane32_swap_b32_e32 v139, v141
	v_permlane32_swap_b32_e32 v134, v136
	v_permlane32_swap_b32_e32 v135, v137
	ds_read_b64_tr_b16 v[64:65], v209 offset:0
	ds_read_b64_tr_b16 v[66:67], v209 offset:0x800
	ds_read_b64_tr_b16 v[68:69], v209 offset:0x1000
	ds_read_b64_tr_b16 v[70:71], v209 offset:0x1800
	ds_read_b64_tr_b16 v[76:77], v209 offset:0x2000
	ds_read_b64_tr_b16 v[78:79], v209 offset:0x2800
	ds_read_b64_tr_b16 v[80:81], v209 offset:0x3000
	ds_read_b64_tr_b16 v[82:83], v209 offset:0x3800
	s_waitcnt lgkmcnt(0)
	s_nop 0
	v_mfma_f32_32x32x16_bf16 v[0:15], v[64:67], v[130:133], v[0:15]
	v_mfma_f32_32x32x16_bf16 v[0:15], v[68:71], v[72:75], v[0:15]
	v_mfma_f32_32x32x16_bf16 v[0:15], v[76:79], v[138:141], v[0:15]
	ds_read_b64_tr_b16 v[64:65], v209 offset:0x200
	ds_read_b64_tr_b16 v[66:67], v209 offset:0xa00
	ds_read_b64_tr_b16 v[68:69], v209 offset:0x1200
	v_mfma_f32_32x32x16_bf16 v[0:15], v[80:83], v[134:137], v[0:15]
	ds_read_b64_tr_b16 v[70:71], v209 offset:0x1a00
	ds_read_b64_tr_b16 v[76:77], v209 offset:0x2200
	ds_read_b64_tr_b16 v[78:79], v209 offset:0x2a00
	ds_read_b64_tr_b16 v[80:81], v209 offset:0x3200
	ds_read_b64_tr_b16 v[82:83], v209 offset:0x3a00
	s_waitcnt lgkmcnt(0)
	v_mfma_f32_32x32x16_bf16 v[48:63], v[64:67], v[130:133], v[48:63]
	v_mfma_f32_32x32x16_bf16 v[48:63], v[68:71], v[72:75], v[48:63]
	v_mfma_f32_32x32x16_bf16 v[48:63], v[76:79], v[138:141], v[48:63]
	v_mov_b32_e32 v128, 1.0
	v_mov_b32_e32 v208, 1.0
	ds_read_b64_tr_b16 v[64:65], v209 offset:0x400
	ds_read_b64_tr_b16 v[66:67], v209 offset:0xc00
	ds_read_b64_tr_b16 v[68:69], v209 offset:0x1400
	v_mfma_f32_32x32x16_bf16 v[48:63], v[80:83], v[134:137], v[48:63]
	ds_read_b64_tr_b16 v[70:71], v209 offset:0x1c00
	ds_read_b64_tr_b16 v[76:77], v209 offset:0x2400
	ds_read_b64_tr_b16 v[78:79], v209 offset:0x2c00
	ds_read_b64_tr_b16 v[80:81], v209 offset:0x3400
	ds_read_b64_tr_b16 v[82:83], v209 offset:0x3c00
	s_waitcnt lgkmcnt(0)
	v_mfma_f32_32x32x16_bf16 v[32:47], v[64:67], v[130:133], v[32:47]
	v_mov_b32_e32 v84, v100
	v_mov_b32_e32 v85, v101
	v_mov_b32_e32 v86, v102
	v_mov_b32_e32 v87, v103
	v_mov_b32_e32 v88, v104
	v_mov_b32_e32 v89, v105
	v_mov_b32_e32 v90, v106
	v_mov_b32_e32 v91, v107
	v_exp_f32_e32 v64, v112
	v_exp_f32_e32 v65, v113
	v_exp_f32_e32 v66, v114
	v_mfma_f32_32x32x16_bf16 v[32:47], v[68:71], v[72:75], v[32:47]
	v_exp_f32_e32 v67, v115
	v_exp_f32_e32 v68, v116
	v_exp_f32_e32 v69, v117
	v_exp_f32_e32 v70, v118
	v_exp_f32_e32 v71, v119
	v_mov_b32_e32 v94, v110
	v_mov_b32_e32 v95, v111
	v_mov_b32_e32 v92, v108
	v_mov_b32_e32 v93, v109
	v_mfma_f32_32x32x16_bf16 v[32:47], v[76:79], v[138:141], v[32:47]
	ds_read_b64_tr_b16 v[76:77], v209 offset:0x600
	ds_read_b64_tr_b16 v[78:79], v209 offset:0xe00
	v_mfma_f32_32x32x16_bf16 v[32:47], v[80:83], v[134:137], v[32:47]
	v_mov_b32_e32 v80, v96
	v_mov_b32_e32 v81, v97
	ds_read_b64_tr_b16 v[96:97], v209 offset:0x1600
	v_mov_b32_e32 v82, v98
	v_mov_b32_e32 v83, v99
	ds_read_b64_tr_b16 v[98:99], v209 offset:0x1e00
	ds_read_b64_tr_b16 v[100:101], v209 offset:0x2600
	ds_read_b64_tr_b16 v[102:103], v209 offset:0x2e00
	ds_read_b64_tr_b16 v[104:105], v209 offset:0x3600
	ds_read_b64_tr_b16 v[106:107], v209 offset:0x3e00
	s_waitcnt lgkmcnt(0)
	v_mfma_f32_32x32x16_bf16 v[16:31], v[76:79], v[130:133], v[16:31]
	v_exp_f32_e32 v76, v124
	v_exp_f32_e32 v77, v125
	v_exp_f32_e32 v78, v126
	v_exp_f32_e32 v79, v127
	v_mfma_f32_32x32x16_bf16 v[16:31], v[96:99], v[72:75], v[16:31]
	v_exp_f32_e32 v72, v120
	v_exp_f32_e32 v73, v121
	v_exp_f32_e32 v74, v122
	v_exp_f32_e32 v75, v123
	s_barrier
	v_mfma_f32_32x32x16_bf16 v[16:31], v[100:103], v[138:141], v[16:31]
	v_mfma_f32_32x32x16_bf16 v[16:31], v[104:107], v[134:137], v[16:31]
	s_branch .LBB0_873
	v_pk_mul_f32 v[14:15], v[14:15], v[128:129] op_sel_hi:[1,0]
	v_pk_mul_f32 v[12:13], v[12:13], v[128:129] op_sel_hi:[1,0]
	v_pk_mul_f32 v[10:11], v[10:11], v[128:129] op_sel_hi:[1,0]
	v_pk_mul_f32 v[8:9], v[8:9], v[128:129] op_sel_hi:[1,0]
	v_pk_mul_f32 v[6:7], v[6:7], v[128:129] op_sel_hi:[1,0]
	v_pk_mul_f32 v[4:5], v[4:5], v[128:129] op_sel_hi:[1,0]
	v_pk_mul_f32 v[2:3], v[2:3], v[128:129] op_sel_hi:[1,0]
	v_pk_mul_f32 v[0:1], v[0:1], v[128:129] op_sel_hi:[1,0]
	v_pk_mul_f32 v[62:63], v[62:63], v[128:129] op_sel_hi:[1,0]
	v_pk_mul_f32 v[60:61], v[60:61], v[128:129] op_sel_hi:[1,0]
	v_pk_mul_f32 v[58:59], v[58:59], v[128:129] op_sel_hi:[1,0]
	v_pk_mul_f32 v[56:57], v[56:57], v[128:129] op_sel_hi:[1,0]
	v_pk_mul_f32 v[54:55], v[54:55], v[128:129] op_sel_hi:[1,0]
	v_pk_mul_f32 v[52:53], v[52:53], v[128:129] op_sel_hi:[1,0]
	v_pk_mul_f32 v[50:51], v[50:51], v[128:129] op_sel_hi:[1,0]
	v_pk_mul_f32 v[48:49], v[48:49], v[128:129] op_sel_hi:[1,0]
	v_pk_mul_f32 v[46:47], v[128:129], v[46:47] op_sel_hi:[0,1]
	v_pk_mul_f32 v[44:45], v[128:129], v[44:45] op_sel_hi:[0,1]
	v_pk_mul_f32 v[42:43], v[128:129], v[42:43] op_sel_hi:[0,1]
	v_pk_mul_f32 v[40:41], v[128:129], v[40:41] op_sel_hi:[0,1]
	v_pk_mul_f32 v[38:39], v[128:129], v[38:39] op_sel_hi:[0,1]
	v_pk_mul_f32 v[36:37], v[128:129], v[36:37] op_sel_hi:[0,1]
	v_pk_mul_f32 v[34:35], v[128:129], v[34:35] op_sel_hi:[0,1]
	v_pk_mul_f32 v[32:33], v[128:129], v[32:33] op_sel_hi:[0,1]
	v_pk_mul_f32 v[30:31], v[128:129], v[30:31] op_sel_hi:[0,1]
	v_pk_mul_f32 v[28:29], v[128:129], v[28:29] op_sel_hi:[0,1]
	v_pk_mul_f32 v[26:27], v[128:129], v[26:27] op_sel_hi:[0,1]
	v_pk_mul_f32 v[24:25], v[128:129], v[24:25] op_sel_hi:[0,1]
	v_pk_mul_f32 v[22:23], v[128:129], v[22:23] op_sel_hi:[0,1]
	v_pk_mul_f32 v[20:21], v[128:129], v[20:21] op_sel_hi:[0,1]
	v_pk_mul_f32 v[18:19], v[128:129], v[18:19] op_sel_hi:[0,1]
	v_pk_mul_f32 v[16:17], v[128:129], v[16:17] op_sel_hi:[0,1]
	s_branch .LBB0_873
